# kv1s_k X-loader rewritten: 6 register sets in flight with counted vmcnt, fully unrolled; comdat section merged into .text
# speedup vs baseline: 1.0129x; 1.0129x over previous
.LBB2_7:
	s_and_b64 vcc, exec, s[12:13]
	s_cbranch_vccz .LBB2_10
	s_cmpk_lt_u32 s2, 0x80
	s_waitcnt lgkmcnt(0)
	s_cselect_b32 s5, s5, s7
	s_cselect_b32 s4, s4, s6
	s_lshl_b32 s6, s15, 20
	s_add_u32 s4, s4, s6
	s_addc_u32 s5, s5, 0
	s_lshl_b32 s6, s14, 2
	s_add_u32 s4, s4, s6
	s_addc_u32 s5, s5, 0
	s_lshl_b32 s6, s3, 5
	s_add_i32 s7, s6, 0xffffff80
	v_or_b32_e32 v2, s7, v1
	v_mov_b32_e32 v3, 0
	v_lshlrev_b64 v[4:5], 14, v[2:3]
	v_or_b32_e32 v133, 20, v2
	v_or_b32_e32 v137, 24, v2
	v_or_b32_e32 v138, 28, v2
	v_lshl_add_u64 v[4:5], s[4:5], 0, v[4:5]
	v_lshlrev_b32_e32 v2, 4, v132
	v_lshl_add_u64 v[130:131], v[4:5], 0, v[2:3]
	v_lshrrev_b32_e32 v132, 3, v132
	s_mov_b64 s[20:21], 0x1000
	v_lshl_add_u64 v[204:205], v[130:131], 0, s[20:21]
	s_mov_b64 s[20:21], 0x11000
	v_lshl_add_u64 v[206:207], v[130:131], 0, s[20:21]
	s_mov_b64 s[20:21], 0x21000
	v_lshl_add_u64 v[208:209], v[130:131], 0, s[20:21]
	s_mov_b64 s[20:21], 0x31000
	v_lshl_add_u64 v[210:211], v[130:131], 0, s[20:21]
	s_mov_b64 s[20:21], 0x41000
	v_lshl_add_u64 v[212:213], v[130:131], 0, s[20:21]
	s_mov_b64 s[20:21], 0x51000
	v_lshl_add_u64 v[214:215], v[130:131], 0, s[20:21]
	s_mov_b64 s[20:21], 0x61000
	v_lshl_add_u64 v[216:217], v[130:131], 0, s[20:21]
	s_mov_b64 s[20:21], 0x71000
	v_lshl_add_u64 v[218:219], v[130:131], 0, s[20:21]
	global_load_dwordx4 v[2:5], v[204:205], off offset:-4096 nt
	global_load_dwordx4 v[6:9], v[206:207], off offset:-4096 nt
	global_load_dwordx4 v[10:13], v[208:209], off offset:-4096 nt
	global_load_dwordx4 v[14:17], v[210:211], off offset:-4096 nt
	global_load_dwordx4 v[18:21], v[212:213], off offset:-4096 nt
	global_load_dwordx4 v[22:25], v[214:215], off offset:-4096 nt
	global_load_dwordx4 v[26:29], v[216:217], off offset:-4096 nt
	global_load_dwordx4 v[30:33], v[218:219], off offset:-4096 nt
	global_load_dwordx4 v[34:37], v[204:205], off offset:-3840 nt
	global_load_dwordx4 v[38:41], v[206:207], off offset:-3840 nt
	global_load_dwordx4 v[42:45], v[208:209], off offset:-3840 nt
	global_load_dwordx4 v[46:49], v[210:211], off offset:-3840 nt
	global_load_dwordx4 v[50:53], v[212:213], off offset:-3840 nt
	global_load_dwordx4 v[54:57], v[214:215], off offset:-3840 nt
	global_load_dwordx4 v[58:61], v[216:217], off offset:-3840 nt
	global_load_dwordx4 v[62:65], v[218:219], off offset:-3840 nt
	global_load_dwordx4 v[66:69], v[204:205], off offset:-3584 nt
	global_load_dwordx4 v[70:73], v[206:207], off offset:-3584 nt
	global_load_dwordx4 v[74:77], v[208:209], off offset:-3584 nt
	global_load_dwordx4 v[78:81], v[210:211], off offset:-3584 nt
	global_load_dwordx4 v[82:85], v[212:213], off offset:-3584 nt
	global_load_dwordx4 v[86:89], v[214:215], off offset:-3584 nt
	global_load_dwordx4 v[90:93], v[216:217], off offset:-3584 nt
	global_load_dwordx4 v[94:97], v[218:219], off offset:-3584 nt
	global_load_dwordx4 v[98:101], v[204:205], off offset:-3328 nt
	global_load_dwordx4 v[102:105], v[206:207], off offset:-3328 nt
	global_load_dwordx4 v[106:109], v[208:209], off offset:-3328 nt
	global_load_dwordx4 v[110:113], v[210:211], off offset:-3328 nt
	global_load_dwordx4 v[114:117], v[212:213], off offset:-3328 nt
	global_load_dwordx4 v[118:121], v[214:215], off offset:-3328 nt
	global_load_dwordx4 v[122:125], v[216:217], off offset:-3328 nt
	global_load_dwordx4 v[126:129], v[218:219], off offset:-3328 nt
	global_load_dwordx4 v[140:143], v[204:205], off offset:-3072 nt
	global_load_dwordx4 v[144:147], v[206:207], off offset:-3072 nt
	global_load_dwordx4 v[148:151], v[208:209], off offset:-3072 nt
	global_load_dwordx4 v[152:155], v[210:211], off offset:-3072 nt
	global_load_dwordx4 v[156:159], v[212:213], off offset:-3072 nt
	global_load_dwordx4 v[160:163], v[214:215], off offset:-3072 nt
	global_load_dwordx4 v[164:167], v[216:217], off offset:-3072 nt
	global_load_dwordx4 v[168:171], v[218:219], off offset:-3072 nt
	global_load_dwordx4 v[172:175], v[204:205], off offset:-2816 nt
	global_load_dwordx4 v[176:179], v[206:207], off offset:-2816 nt
	global_load_dwordx4 v[180:183], v[208:209], off offset:-2816 nt
	global_load_dwordx4 v[184:187], v[210:211], off offset:-2816 nt
	global_load_dwordx4 v[188:191], v[212:213], off offset:-2816 nt
	global_load_dwordx4 v[192:195], v[214:215], off offset:-2816 nt
	global_load_dwordx4 v[196:199], v[216:217], off offset:-2816 nt
	global_load_dwordx4 v[200:203], v[218:219], off offset:-2816 nt
	v_lshlrev_b32_e32 v135, 3, v0
	s_lshr_b32 s4, s7, 3
	s_addk_i32 s6, 0xff90
	v_and_b32_e32 v139, 56, v135
	v_or_b32_e32 v135, s4, v132
	s_lshr_b32 s4, s6, 3
	v_or_b32_e32 v136, s4, v132
	v_lshl_or_b32 v1, v1, 6, v139
	v_lshl_or_b32 v1, v136, 10, v1
	v_lshrrev_b32_e32 v136, 3, v133
	v_lshlrev_b32_e32 v133, 6, v133
	s_movk_i32 s4, 0x1c0
	v_or_b32_e32 v136, v136, v132
	v_and_or_b32 v133, v133, s4, v139
	v_lshl_or_b32 v133, v136, 10, v133
	v_add_u32_e32 v136, 0x18000, v133
	v_lshrrev_b32_e32 v133, 3, v137
	s_mov_b32 s4, 0x3ffffe
	v_and_or_b32 v133, v133, s4, v132
	v_lshlrev_b32_e32 v137, 6, v137
	v_and_b32_e32 v137, 0x2c0, v137
	v_lshlrev_b32_e32 v133, 10, v133
	v_or3_b32 v133, v133, v137, v139
	v_add_u32_e32 v133, 0x18000, v133
	v_lshrrev_b32_e32 v134, 4, v0
	v_xor_b32_e32 v137, 32, v133
	v_lshrrev_b32_e32 v133, 3, v138
	v_lshlrev_b32_e32 v134, 6, v134
	v_and_or_b32 v132, v133, s4, v132
	v_lshlrev_b32_e32 v133, 6, v138
	v_and_b32_e32 v134, 0xc0, v134
	v_lshlrev_b32_e32 v135, 10, v135
	v_and_b32_e32 v133, 0x3c0, v133
	v_lshlrev_b32_e32 v132, 10, v132
	v_or3_b32 v135, v135, v134, v139
	v_or3_b32 v132, v132, v133, v139
	v_add_u32_e32 v134, 0x18000, v135
	v_add_u32_e32 v132, 0x18000, v132
	v_add_u32_e32 v135, 0x18100, v135
	v_add_u32_e32 v1, 0x18000, v1
	v_xor_b32_e32 v138, 32, v132
	v_xor_b32_e32 v139, 32, v134
	s_waitcnt vmcnt(40)
	v_cvt_pk_f16_f32 v2, v2, v3
	v_cvt_pk_f16_f32 v3, v4, v5
	v_cvt_pk_f16_f32 v6, v6, v7
	v_cvt_pk_f16_f32 v7, v8, v9
	v_cvt_pk_f16_f32 v10, v10, v11
	v_cvt_pk_f16_f32 v11, v12, v13
	v_cvt_pk_f16_f32 v14, v14, v15
	v_cvt_pk_f16_f32 v15, v16, v17
	v_cvt_pk_f16_f32 v18, v18, v19
	v_cvt_pk_f16_f32 v19, v20, v21
	v_cvt_pk_f16_f32 v22, v22, v23
	v_cvt_pk_f16_f32 v23, v24, v25
	v_cvt_pk_f16_f32 v26, v26, v27
	v_cvt_pk_f16_f32 v27, v28, v29
	v_cvt_pk_f16_f32 v30, v30, v31
	v_cvt_pk_f16_f32 v31, v32, v33
	ds_write_b64 v134, v[2:3]
	ds_write_b64 v135, v[6:7]
	ds_write_b64 v139, v[10:11] offset:512
	ds_write_b64 v139, v[14:15] offset:768
	ds_write_b64 v1, v[18:19]
	ds_write_b64 v136, v[22:23]
	ds_write_b64 v137, v[26:27]
	ds_write_b64 v138, v[30:31]
	global_load_dwordx4 v[2:5], v[204:205], off offset:-2560 nt
	global_load_dwordx4 v[6:9], v[206:207], off offset:-2560 nt
	global_load_dwordx4 v[10:13], v[208:209], off offset:-2560 nt
	global_load_dwordx4 v[14:17], v[210:211], off offset:-2560 nt
	global_load_dwordx4 v[18:21], v[212:213], off offset:-2560 nt
	global_load_dwordx4 v[22:25], v[214:215], off offset:-2560 nt
	global_load_dwordx4 v[26:29], v[216:217], off offset:-2560 nt
	global_load_dwordx4 v[30:33], v[218:219], off offset:-2560 nt
	s_waitcnt lgkmcnt(0)
	s_barrier
	s_waitcnt vmcnt(40)
	v_cvt_pk_f16_f32 v34, v34, v35
	v_cvt_pk_f16_f32 v35, v36, v37
	v_cvt_pk_f16_f32 v38, v38, v39
	v_cvt_pk_f16_f32 v39, v40, v41
	v_cvt_pk_f16_f32 v42, v42, v43
	v_cvt_pk_f16_f32 v43, v44, v45
	v_cvt_pk_f16_f32 v46, v46, v47
	v_cvt_pk_f16_f32 v47, v48, v49
	v_cvt_pk_f16_f32 v50, v50, v51
	v_cvt_pk_f16_f32 v51, v52, v53
	v_cvt_pk_f16_f32 v54, v54, v55
	v_cvt_pk_f16_f32 v55, v56, v57
	v_cvt_pk_f16_f32 v58, v58, v59
	v_cvt_pk_f16_f32 v59, v60, v61
	v_cvt_pk_f16_f32 v62, v62, v63
	v_cvt_pk_f16_f32 v63, v64, v65
	ds_write_b64 v134, v[34:35] offset:8192
	ds_write_b64 v135, v[38:39] offset:8192
	ds_write_b64 v139, v[42:43] offset:8704
	ds_write_b64 v139, v[46:47] offset:8960
	ds_write_b64 v1, v[50:51] offset:8192
	ds_write_b64 v136, v[54:55] offset:8192
	ds_write_b64 v137, v[58:59] offset:8192
	ds_write_b64 v138, v[62:63] offset:8192
	global_load_dwordx4 v[34:37], v[204:205], off offset:-2304 nt
	global_load_dwordx4 v[38:41], v[206:207], off offset:-2304 nt
	global_load_dwordx4 v[42:45], v[208:209], off offset:-2304 nt
	global_load_dwordx4 v[46:49], v[210:211], off offset:-2304 nt
	global_load_dwordx4 v[50:53], v[212:213], off offset:-2304 nt
	global_load_dwordx4 v[54:57], v[214:215], off offset:-2304 nt
	global_load_dwordx4 v[58:61], v[216:217], off offset:-2304 nt
	global_load_dwordx4 v[62:65], v[218:219], off offset:-2304 nt
	s_waitcnt lgkmcnt(0)
	s_barrier
	s_waitcnt vmcnt(40)
	v_cvt_pk_f16_f32 v66, v66, v67
	v_cvt_pk_f16_f32 v67, v68, v69
	v_cvt_pk_f16_f32 v70, v70, v71
	v_cvt_pk_f16_f32 v71, v72, v73
	v_cvt_pk_f16_f32 v74, v74, v75
	v_cvt_pk_f16_f32 v75, v76, v77
	v_cvt_pk_f16_f32 v78, v78, v79
	v_cvt_pk_f16_f32 v79, v80, v81
	v_cvt_pk_f16_f32 v82, v82, v83
	v_cvt_pk_f16_f32 v83, v84, v85
	v_cvt_pk_f16_f32 v86, v86, v87
	v_cvt_pk_f16_f32 v87, v88, v89
	v_cvt_pk_f16_f32 v90, v90, v91
	v_cvt_pk_f16_f32 v91, v92, v93
	v_cvt_pk_f16_f32 v94, v94, v95
	v_cvt_pk_f16_f32 v95, v96, v97
	ds_write_b64 v134, v[66:67] offset:16384
	ds_write_b64 v135, v[70:71] offset:16384
	ds_write_b64 v139, v[74:75] offset:16896
	ds_write_b64 v139, v[78:79] offset:17152
	ds_write_b64 v1, v[82:83] offset:16384
	ds_write_b64 v136, v[86:87] offset:16384
	ds_write_b64 v137, v[90:91] offset:16384
	ds_write_b64 v138, v[94:95] offset:16384
	global_load_dwordx4 v[66:69], v[204:205], off offset:-2048 nt
	global_load_dwordx4 v[70:73], v[206:207], off offset:-2048 nt
	global_load_dwordx4 v[74:77], v[208:209], off offset:-2048 nt
	global_load_dwordx4 v[78:81], v[210:211], off offset:-2048 nt
	global_load_dwordx4 v[82:85], v[212:213], off offset:-2048 nt
	global_load_dwordx4 v[86:89], v[214:215], off offset:-2048 nt
	global_load_dwordx4 v[90:93], v[216:217], off offset:-2048 nt
	global_load_dwordx4 v[94:97], v[218:219], off offset:-2048 nt
	s_waitcnt lgkmcnt(0)
	s_barrier
	s_waitcnt vmcnt(40)
	v_cvt_pk_f16_f32 v98, v98, v99
	v_cvt_pk_f16_f32 v99, v100, v101
	v_cvt_pk_f16_f32 v102, v102, v103
	v_cvt_pk_f16_f32 v103, v104, v105
	v_cvt_pk_f16_f32 v106, v106, v107
	v_cvt_pk_f16_f32 v107, v108, v109
	v_cvt_pk_f16_f32 v110, v110, v111
	v_cvt_pk_f16_f32 v111, v112, v113
	v_cvt_pk_f16_f32 v114, v114, v115
	v_cvt_pk_f16_f32 v115, v116, v117
	v_cvt_pk_f16_f32 v118, v118, v119
	v_cvt_pk_f16_f32 v119, v120, v121
	v_cvt_pk_f16_f32 v122, v122, v123
	v_cvt_pk_f16_f32 v123, v124, v125
	v_cvt_pk_f16_f32 v126, v126, v127
	v_cvt_pk_f16_f32 v127, v128, v129
	ds_write_b64 v134, v[98:99]
	ds_write_b64 v135, v[102:103]
	ds_write_b64 v139, v[106:107] offset:512
	ds_write_b64 v139, v[110:111] offset:768
	ds_write_b64 v1, v[114:115]
	ds_write_b64 v136, v[118:119]
	ds_write_b64 v137, v[122:123]
	ds_write_b64 v138, v[126:127]
	global_load_dwordx4 v[98:101], v[204:205], off offset:-1792 nt
	global_load_dwordx4 v[102:105], v[206:207], off offset:-1792 nt
	global_load_dwordx4 v[106:109], v[208:209], off offset:-1792 nt
	global_load_dwordx4 v[110:113], v[210:211], off offset:-1792 nt
	global_load_dwordx4 v[114:117], v[212:213], off offset:-1792 nt
	global_load_dwordx4 v[118:121], v[214:215], off offset:-1792 nt
	global_load_dwordx4 v[122:125], v[216:217], off offset:-1792 nt
	global_load_dwordx4 v[126:129], v[218:219], off offset:-1792 nt
	s_waitcnt lgkmcnt(0)
	s_barrier
	s_waitcnt vmcnt(40)
	v_cvt_pk_f16_f32 v140, v140, v141
	v_cvt_pk_f16_f32 v141, v142, v143
	v_cvt_pk_f16_f32 v144, v144, v145
	v_cvt_pk_f16_f32 v145, v146, v147
	v_cvt_pk_f16_f32 v148, v148, v149
	v_cvt_pk_f16_f32 v149, v150, v151
	v_cvt_pk_f16_f32 v152, v152, v153
	v_cvt_pk_f16_f32 v153, v154, v155
	v_cvt_pk_f16_f32 v156, v156, v157
	v_cvt_pk_f16_f32 v157, v158, v159
	v_cvt_pk_f16_f32 v160, v160, v161
	v_cvt_pk_f16_f32 v161, v162, v163
	v_cvt_pk_f16_f32 v164, v164, v165
	v_cvt_pk_f16_f32 v165, v166, v167
	v_cvt_pk_f16_f32 v168, v168, v169
	v_cvt_pk_f16_f32 v169, v170, v171
	ds_write_b64 v134, v[140:141] offset:8192
	ds_write_b64 v135, v[144:145] offset:8192
	ds_write_b64 v139, v[148:149] offset:8704
	ds_write_b64 v139, v[152:153] offset:8960
	ds_write_b64 v1, v[156:157] offset:8192
	ds_write_b64 v136, v[160:161] offset:8192
	ds_write_b64 v137, v[164:165] offset:8192
	ds_write_b64 v138, v[168:169] offset:8192
	global_load_dwordx4 v[140:143], v[204:205], off offset:-1536 nt
	global_load_dwordx4 v[144:147], v[206:207], off offset:-1536 nt
	global_load_dwordx4 v[148:151], v[208:209], off offset:-1536 nt
	global_load_dwordx4 v[152:155], v[210:211], off offset:-1536 nt
	global_load_dwordx4 v[156:159], v[212:213], off offset:-1536 nt
	global_load_dwordx4 v[160:163], v[214:215], off offset:-1536 nt
	global_load_dwordx4 v[164:167], v[216:217], off offset:-1536 nt
	global_load_dwordx4 v[168:171], v[218:219], off offset:-1536 nt
	s_waitcnt lgkmcnt(0)
	s_barrier
	s_waitcnt vmcnt(40)
	v_cvt_pk_f16_f32 v172, v172, v173
	v_cvt_pk_f16_f32 v173, v174, v175
	v_cvt_pk_f16_f32 v176, v176, v177
	v_cvt_pk_f16_f32 v177, v178, v179
	v_cvt_pk_f16_f32 v180, v180, v181
	v_cvt_pk_f16_f32 v181, v182, v183
	v_cvt_pk_f16_f32 v184, v184, v185
	v_cvt_pk_f16_f32 v185, v186, v187
	v_cvt_pk_f16_f32 v188, v188, v189
	v_cvt_pk_f16_f32 v189, v190, v191
	v_cvt_pk_f16_f32 v192, v192, v193
	v_cvt_pk_f16_f32 v193, v194, v195
	v_cvt_pk_f16_f32 v196, v196, v197
	v_cvt_pk_f16_f32 v197, v198, v199
	v_cvt_pk_f16_f32 v200, v200, v201
	v_cvt_pk_f16_f32 v201, v202, v203
	ds_write_b64 v134, v[172:173] offset:16384
	ds_write_b64 v135, v[176:177] offset:16384
	ds_write_b64 v139, v[180:181] offset:16896
	ds_write_b64 v139, v[184:185] offset:17152
	ds_write_b64 v1, v[188:189] offset:16384
	ds_write_b64 v136, v[192:193] offset:16384
	ds_write_b64 v137, v[196:197] offset:16384
	ds_write_b64 v138, v[200:201] offset:16384
	global_load_dwordx4 v[172:175], v[204:205], off offset:-1280 nt
	global_load_dwordx4 v[176:179], v[206:207], off offset:-1280 nt
	global_load_dwordx4 v[180:183], v[208:209], off offset:-1280 nt
	global_load_dwordx4 v[184:187], v[210:211], off offset:-1280 nt
	global_load_dwordx4 v[188:191], v[212:213], off offset:-1280 nt
	global_load_dwordx4 v[192:195], v[214:215], off offset:-1280 nt
	global_load_dwordx4 v[196:199], v[216:217], off offset:-1280 nt
	global_load_dwordx4 v[200:203], v[218:219], off offset:-1280 nt
	s_waitcnt lgkmcnt(0)
	s_barrier
	s_waitcnt vmcnt(40)
	v_cvt_pk_f16_f32 v2, v2, v3
	v_cvt_pk_f16_f32 v3, v4, v5
	v_cvt_pk_f16_f32 v6, v6, v7
	v_cvt_pk_f16_f32 v7, v8, v9
	v_cvt_pk_f16_f32 v10, v10, v11
	v_cvt_pk_f16_f32 v11, v12, v13
	v_cvt_pk_f16_f32 v14, v14, v15
	v_cvt_pk_f16_f32 v15, v16, v17
	v_cvt_pk_f16_f32 v18, v18, v19
	v_cvt_pk_f16_f32 v19, v20, v21
	v_cvt_pk_f16_f32 v22, v22, v23
	v_cvt_pk_f16_f32 v23, v24, v25
	v_cvt_pk_f16_f32 v26, v26, v27
	v_cvt_pk_f16_f32 v27, v28, v29
	v_cvt_pk_f16_f32 v30, v30, v31
	v_cvt_pk_f16_f32 v31, v32, v33
	ds_write_b64 v134, v[2:3]
	ds_write_b64 v135, v[6:7]
	ds_write_b64 v139, v[10:11] offset:512
	ds_write_b64 v139, v[14:15] offset:768
	ds_write_b64 v1, v[18:19]
	ds_write_b64 v136, v[22:23]
	ds_write_b64 v137, v[26:27]
	ds_write_b64 v138, v[30:31]
	global_load_dwordx4 v[2:5], v[204:205], off offset:-1024 nt
	global_load_dwordx4 v[6:9], v[206:207], off offset:-1024 nt
	global_load_dwordx4 v[10:13], v[208:209], off offset:-1024 nt
	global_load_dwordx4 v[14:17], v[210:211], off offset:-1024 nt
	global_load_dwordx4 v[18:21], v[212:213], off offset:-1024 nt
	global_load_dwordx4 v[22:25], v[214:215], off offset:-1024 nt
	global_load_dwordx4 v[26:29], v[216:217], off offset:-1024 nt
	global_load_dwordx4 v[30:33], v[218:219], off offset:-1024 nt
	s_waitcnt lgkmcnt(0)
	s_barrier
	s_waitcnt vmcnt(40)
	v_cvt_pk_f16_f32 v34, v34, v35
	v_cvt_pk_f16_f32 v35, v36, v37
	v_cvt_pk_f16_f32 v38, v38, v39
	v_cvt_pk_f16_f32 v39, v40, v41
	v_cvt_pk_f16_f32 v42, v42, v43
	v_cvt_pk_f16_f32 v43, v44, v45
	v_cvt_pk_f16_f32 v46, v46, v47
	v_cvt_pk_f16_f32 v47, v48, v49
	v_cvt_pk_f16_f32 v50, v50, v51
	v_cvt_pk_f16_f32 v51, v52, v53
	v_cvt_pk_f16_f32 v54, v54, v55
	v_cvt_pk_f16_f32 v55, v56, v57
	v_cvt_pk_f16_f32 v58, v58, v59
	v_cvt_pk_f16_f32 v59, v60, v61
	v_cvt_pk_f16_f32 v62, v62, v63
	v_cvt_pk_f16_f32 v63, v64, v65
	ds_write_b64 v134, v[34:35] offset:8192
	ds_write_b64 v135, v[38:39] offset:8192
	ds_write_b64 v139, v[42:43] offset:8704
	ds_write_b64 v139, v[46:47] offset:8960
	ds_write_b64 v1, v[50:51] offset:8192
	ds_write_b64 v136, v[54:55] offset:8192
	ds_write_b64 v137, v[58:59] offset:8192
	ds_write_b64 v138, v[62:63] offset:8192
	global_load_dwordx4 v[34:37], v[204:205], off offset:-768 nt
	global_load_dwordx4 v[38:41], v[206:207], off offset:-768 nt
	global_load_dwordx4 v[42:45], v[208:209], off offset:-768 nt
	global_load_dwordx4 v[46:49], v[210:211], off offset:-768 nt
	global_load_dwordx4 v[50:53], v[212:213], off offset:-768 nt
	global_load_dwordx4 v[54:57], v[214:215], off offset:-768 nt
	global_load_dwordx4 v[58:61], v[216:217], off offset:-768 nt
	global_load_dwordx4 v[62:65], v[218:219], off offset:-768 nt
	s_waitcnt lgkmcnt(0)
	s_barrier
	s_waitcnt vmcnt(40)
	v_cvt_pk_f16_f32 v66, v66, v67
	v_cvt_pk_f16_f32 v67, v68, v69
	v_cvt_pk_f16_f32 v70, v70, v71
	v_cvt_pk_f16_f32 v71, v72, v73
	v_cvt_pk_f16_f32 v74, v74, v75
	v_cvt_pk_f16_f32 v75, v76, v77
	v_cvt_pk_f16_f32 v78, v78, v79
	v_cvt_pk_f16_f32 v79, v80, v81
	v_cvt_pk_f16_f32 v82, v82, v83
	v_cvt_pk_f16_f32 v83, v84, v85
	v_cvt_pk_f16_f32 v86, v86, v87
	v_cvt_pk_f16_f32 v87, v88, v89
	v_cvt_pk_f16_f32 v90, v90, v91
	v_cvt_pk_f16_f32 v91, v92, v93
	v_cvt_pk_f16_f32 v94, v94, v95
	v_cvt_pk_f16_f32 v95, v96, v97
	ds_write_b64 v134, v[66:67] offset:16384
	ds_write_b64 v135, v[70:71] offset:16384
	ds_write_b64 v139, v[74:75] offset:16896
	ds_write_b64 v139, v[78:79] offset:17152
	ds_write_b64 v1, v[82:83] offset:16384
	ds_write_b64 v136, v[86:87] offset:16384
	ds_write_b64 v137, v[90:91] offset:16384
	ds_write_b64 v138, v[94:95] offset:16384
	global_load_dwordx4 v[66:69], v[204:205], off offset:-512 nt
	global_load_dwordx4 v[70:73], v[206:207], off offset:-512 nt
	global_load_dwordx4 v[74:77], v[208:209], off offset:-512 nt
	global_load_dwordx4 v[78:81], v[210:211], off offset:-512 nt
	global_load_dwordx4 v[82:85], v[212:213], off offset:-512 nt
	global_load_dwordx4 v[86:89], v[214:215], off offset:-512 nt
	global_load_dwordx4 v[90:93], v[216:217], off offset:-512 nt
	global_load_dwordx4 v[94:97], v[218:219], off offset:-512 nt
	s_waitcnt lgkmcnt(0)
	s_barrier
	s_waitcnt vmcnt(40)
	v_cvt_pk_f16_f32 v98, v98, v99
	v_cvt_pk_f16_f32 v99, v100, v101
	v_cvt_pk_f16_f32 v102, v102, v103
	v_cvt_pk_f16_f32 v103, v104, v105
	v_cvt_pk_f16_f32 v106, v106, v107
	v_cvt_pk_f16_f32 v107, v108, v109
	v_cvt_pk_f16_f32 v110, v110, v111
	v_cvt_pk_f16_f32 v111, v112, v113
	v_cvt_pk_f16_f32 v114, v114, v115
	v_cvt_pk_f16_f32 v115, v116, v117
	v_cvt_pk_f16_f32 v118, v118, v119
	v_cvt_pk_f16_f32 v119, v120, v121
	v_cvt_pk_f16_f32 v122, v122, v123
	v_cvt_pk_f16_f32 v123, v124, v125
	v_cvt_pk_f16_f32 v126, v126, v127
	v_cvt_pk_f16_f32 v127, v128, v129
	ds_write_b64 v134, v[98:99]
	ds_write_b64 v135, v[102:103]
	ds_write_b64 v139, v[106:107] offset:512
	ds_write_b64 v139, v[110:111] offset:768
	ds_write_b64 v1, v[114:115]
	ds_write_b64 v136, v[118:119]
	ds_write_b64 v137, v[122:123]
	ds_write_b64 v138, v[126:127]
	global_load_dwordx4 v[98:101], v[204:205], off offset:-256 nt
	global_load_dwordx4 v[102:105], v[206:207], off offset:-256 nt
	global_load_dwordx4 v[106:109], v[208:209], off offset:-256 nt
	global_load_dwordx4 v[110:113], v[210:211], off offset:-256 nt
	global_load_dwordx4 v[114:117], v[212:213], off offset:-256 nt
	global_load_dwordx4 v[118:121], v[214:215], off offset:-256 nt
	global_load_dwordx4 v[122:125], v[216:217], off offset:-256 nt
	global_load_dwordx4 v[126:129], v[218:219], off offset:-256 nt
	s_waitcnt lgkmcnt(0)
	s_barrier
	s_waitcnt vmcnt(40)
	v_cvt_pk_f16_f32 v140, v140, v141
	v_cvt_pk_f16_f32 v141, v142, v143
	v_cvt_pk_f16_f32 v144, v144, v145
	v_cvt_pk_f16_f32 v145, v146, v147
	v_cvt_pk_f16_f32 v148, v148, v149
	v_cvt_pk_f16_f32 v149, v150, v151
	v_cvt_pk_f16_f32 v152, v152, v153
	v_cvt_pk_f16_f32 v153, v154, v155
	v_cvt_pk_f16_f32 v156, v156, v157
	v_cvt_pk_f16_f32 v157, v158, v159
	v_cvt_pk_f16_f32 v160, v160, v161
	v_cvt_pk_f16_f32 v161, v162, v163
	v_cvt_pk_f16_f32 v164, v164, v165
	v_cvt_pk_f16_f32 v165, v166, v167
	v_cvt_pk_f16_f32 v168, v168, v169
	v_cvt_pk_f16_f32 v169, v170, v171
	ds_write_b64 v134, v[140:141] offset:8192
	ds_write_b64 v135, v[144:145] offset:8192
	ds_write_b64 v139, v[148:149] offset:8704
	ds_write_b64 v139, v[152:153] offset:8960
	ds_write_b64 v1, v[156:157] offset:8192
	ds_write_b64 v136, v[160:161] offset:8192
	ds_write_b64 v137, v[164:165] offset:8192
	ds_write_b64 v138, v[168:169] offset:8192
	global_load_dwordx4 v[140:143], v[204:205], off offset:0 nt
	global_load_dwordx4 v[144:147], v[206:207], off offset:0 nt
	global_load_dwordx4 v[148:151], v[208:209], off offset:0 nt
	global_load_dwordx4 v[152:155], v[210:211], off offset:0 nt
	global_load_dwordx4 v[156:159], v[212:213], off offset:0 nt
	global_load_dwordx4 v[160:163], v[214:215], off offset:0 nt
	global_load_dwordx4 v[164:167], v[216:217], off offset:0 nt
	global_load_dwordx4 v[168:171], v[218:219], off offset:0 nt
	s_waitcnt lgkmcnt(0)
	s_barrier
	s_waitcnt vmcnt(40)
	v_cvt_pk_f16_f32 v172, v172, v173
	v_cvt_pk_f16_f32 v173, v174, v175
	v_cvt_pk_f16_f32 v176, v176, v177
	v_cvt_pk_f16_f32 v177, v178, v179
	v_cvt_pk_f16_f32 v180, v180, v181
	v_cvt_pk_f16_f32 v181, v182, v183
	v_cvt_pk_f16_f32 v184, v184, v185
	v_cvt_pk_f16_f32 v185, v186, v187
	v_cvt_pk_f16_f32 v188, v188, v189
	v_cvt_pk_f16_f32 v189, v190, v191
	v_cvt_pk_f16_f32 v192, v192, v193
	v_cvt_pk_f16_f32 v193, v194, v195
	v_cvt_pk_f16_f32 v196, v196, v197
	v_cvt_pk_f16_f32 v197, v198, v199
	v_cvt_pk_f16_f32 v200, v200, v201
	v_cvt_pk_f16_f32 v201, v202, v203
	ds_write_b64 v134, v[172:173] offset:16384
	ds_write_b64 v135, v[176:177] offset:16384
	ds_write_b64 v139, v[180:181] offset:16896
	ds_write_b64 v139, v[184:185] offset:17152
	ds_write_b64 v1, v[188:189] offset:16384
	ds_write_b64 v136, v[192:193] offset:16384
	ds_write_b64 v137, v[196:197] offset:16384
	ds_write_b64 v138, v[200:201] offset:16384
	global_load_dwordx4 v[172:175], v[204:205], off offset:256 nt
	global_load_dwordx4 v[176:179], v[206:207], off offset:256 nt
	global_load_dwordx4 v[180:183], v[208:209], off offset:256 nt
	global_load_dwordx4 v[184:187], v[210:211], off offset:256 nt
	global_load_dwordx4 v[188:191], v[212:213], off offset:256 nt
	global_load_dwordx4 v[192:195], v[214:215], off offset:256 nt
	global_load_dwordx4 v[196:199], v[216:217], off offset:256 nt
	global_load_dwordx4 v[200:203], v[218:219], off offset:256 nt
	s_waitcnt lgkmcnt(0)
	s_barrier
	s_waitcnt vmcnt(40)
	v_cvt_pk_f16_f32 v2, v2, v3
	v_cvt_pk_f16_f32 v3, v4, v5
	v_cvt_pk_f16_f32 v6, v6, v7
	v_cvt_pk_f16_f32 v7, v8, v9
	v_cvt_pk_f16_f32 v10, v10, v11
	v_cvt_pk_f16_f32 v11, v12, v13
	v_cvt_pk_f16_f32 v14, v14, v15
	v_cvt_pk_f16_f32 v15, v16, v17
	v_cvt_pk_f16_f32 v18, v18, v19
	v_cvt_pk_f16_f32 v19, v20, v21
	v_cvt_pk_f16_f32 v22, v22, v23
	v_cvt_pk_f16_f32 v23, v24, v25
	v_cvt_pk_f16_f32 v26, v26, v27
	v_cvt_pk_f16_f32 v27, v28, v29
	v_cvt_pk_f16_f32 v30, v30, v31
	v_cvt_pk_f16_f32 v31, v32, v33
	ds_write_b64 v134, v[2:3]
	ds_write_b64 v135, v[6:7]
	ds_write_b64 v139, v[10:11] offset:512
	ds_write_b64 v139, v[14:15] offset:768
	ds_write_b64 v1, v[18:19]
	ds_write_b64 v136, v[22:23]
	ds_write_b64 v137, v[26:27]
	ds_write_b64 v138, v[30:31]
	global_load_dwordx4 v[2:5], v[204:205], off offset:512 nt
	global_load_dwordx4 v[6:9], v[206:207], off offset:512 nt
	global_load_dwordx4 v[10:13], v[208:209], off offset:512 nt
	global_load_dwordx4 v[14:17], v[210:211], off offset:512 nt
	global_load_dwordx4 v[18:21], v[212:213], off offset:512 nt
	global_load_dwordx4 v[22:25], v[214:215], off offset:512 nt
	global_load_dwordx4 v[26:29], v[216:217], off offset:512 nt
	global_load_dwordx4 v[30:33], v[218:219], off offset:512 nt
	s_waitcnt lgkmcnt(0)
	s_barrier
	s_waitcnt vmcnt(40)
	v_cvt_pk_f16_f32 v34, v34, v35
	v_cvt_pk_f16_f32 v35, v36, v37
	v_cvt_pk_f16_f32 v38, v38, v39
	v_cvt_pk_f16_f32 v39, v40, v41
	v_cvt_pk_f16_f32 v42, v42, v43
	v_cvt_pk_f16_f32 v43, v44, v45
	v_cvt_pk_f16_f32 v46, v46, v47
	v_cvt_pk_f16_f32 v47, v48, v49
	v_cvt_pk_f16_f32 v50, v50, v51
	v_cvt_pk_f16_f32 v51, v52, v53
	v_cvt_pk_f16_f32 v54, v54, v55
	v_cvt_pk_f16_f32 v55, v56, v57
	v_cvt_pk_f16_f32 v58, v58, v59
	v_cvt_pk_f16_f32 v59, v60, v61
	v_cvt_pk_f16_f32 v62, v62, v63
	v_cvt_pk_f16_f32 v63, v64, v65
	ds_write_b64 v134, v[34:35] offset:8192
	ds_write_b64 v135, v[38:39] offset:8192
	ds_write_b64 v139, v[42:43] offset:8704
	ds_write_b64 v139, v[46:47] offset:8960
	ds_write_b64 v1, v[50:51] offset:8192
	ds_write_b64 v136, v[54:55] offset:8192
	ds_write_b64 v137, v[58:59] offset:8192
	ds_write_b64 v138, v[62:63] offset:8192
	global_load_dwordx4 v[34:37], v[204:205], off offset:768 nt
	global_load_dwordx4 v[38:41], v[206:207], off offset:768 nt
	global_load_dwordx4 v[42:45], v[208:209], off offset:768 nt
	global_load_dwordx4 v[46:49], v[210:211], off offset:768 nt
	global_load_dwordx4 v[50:53], v[212:213], off offset:768 nt
	global_load_dwordx4 v[54:57], v[214:215], off offset:768 nt
	global_load_dwordx4 v[58:61], v[216:217], off offset:768 nt
	global_load_dwordx4 v[62:65], v[218:219], off offset:768 nt
	s_waitcnt lgkmcnt(0)
	s_barrier
	s_waitcnt vmcnt(40)
	v_cvt_pk_f16_f32 v66, v66, v67
	v_cvt_pk_f16_f32 v67, v68, v69
	v_cvt_pk_f16_f32 v70, v70, v71
	v_cvt_pk_f16_f32 v71, v72, v73
	v_cvt_pk_f16_f32 v74, v74, v75
	v_cvt_pk_f16_f32 v75, v76, v77
	v_cvt_pk_f16_f32 v78, v78, v79
	v_cvt_pk_f16_f32 v79, v80, v81
	v_cvt_pk_f16_f32 v82, v82, v83
	v_cvt_pk_f16_f32 v83, v84, v85
	v_cvt_pk_f16_f32 v86, v86, v87
	v_cvt_pk_f16_f32 v87, v88, v89
	v_cvt_pk_f16_f32 v90, v90, v91
	v_cvt_pk_f16_f32 v91, v92, v93
	v_cvt_pk_f16_f32 v94, v94, v95
	v_cvt_pk_f16_f32 v95, v96, v97
	ds_write_b64 v134, v[66:67] offset:16384
	ds_write_b64 v135, v[70:71] offset:16384
	ds_write_b64 v139, v[74:75] offset:16896
	ds_write_b64 v139, v[78:79] offset:17152
	ds_write_b64 v1, v[82:83] offset:16384
	ds_write_b64 v136, v[86:87] offset:16384
	ds_write_b64 v137, v[90:91] offset:16384
	ds_write_b64 v138, v[94:95] offset:16384
	global_load_dwordx4 v[66:69], v[204:205], off offset:1024 nt
	global_load_dwordx4 v[70:73], v[206:207], off offset:1024 nt
	global_load_dwordx4 v[74:77], v[208:209], off offset:1024 nt
	global_load_dwordx4 v[78:81], v[210:211], off offset:1024 nt
	global_load_dwordx4 v[82:85], v[212:213], off offset:1024 nt
	global_load_dwordx4 v[86:89], v[214:215], off offset:1024 nt
	global_load_dwordx4 v[90:93], v[216:217], off offset:1024 nt
	global_load_dwordx4 v[94:97], v[218:219], off offset:1024 nt
	s_waitcnt lgkmcnt(0)
	s_barrier
	s_waitcnt vmcnt(40)
	v_cvt_pk_f16_f32 v98, v98, v99
	v_cvt_pk_f16_f32 v99, v100, v101
	v_cvt_pk_f16_f32 v102, v102, v103
	v_cvt_pk_f16_f32 v103, v104, v105
	v_cvt_pk_f16_f32 v106, v106, v107
	v_cvt_pk_f16_f32 v107, v108, v109
	v_cvt_pk_f16_f32 v110, v110, v111
	v_cvt_pk_f16_f32 v111, v112, v113
	v_cvt_pk_f16_f32 v114, v114, v115
	v_cvt_pk_f16_f32 v115, v116, v117
	v_cvt_pk_f16_f32 v118, v118, v119
	v_cvt_pk_f16_f32 v119, v120, v121
	v_cvt_pk_f16_f32 v122, v122, v123
	v_cvt_pk_f16_f32 v123, v124, v125
	v_cvt_pk_f16_f32 v126, v126, v127
	v_cvt_pk_f16_f32 v127, v128, v129
	ds_write_b64 v134, v[98:99]
	ds_write_b64 v135, v[102:103]
	ds_write_b64 v139, v[106:107] offset:512
	ds_write_b64 v139, v[110:111] offset:768
	ds_write_b64 v1, v[114:115]
	ds_write_b64 v136, v[118:119]
	ds_write_b64 v137, v[122:123]
	ds_write_b64 v138, v[126:127]
	global_load_dwordx4 v[98:101], v[204:205], off offset:1280 nt
	global_load_dwordx4 v[102:105], v[206:207], off offset:1280 nt
	global_load_dwordx4 v[106:109], v[208:209], off offset:1280 nt
	global_load_dwordx4 v[110:113], v[210:211], off offset:1280 nt
	global_load_dwordx4 v[114:117], v[212:213], off offset:1280 nt
	global_load_dwordx4 v[118:121], v[214:215], off offset:1280 nt
	global_load_dwordx4 v[122:125], v[216:217], off offset:1280 nt
	global_load_dwordx4 v[126:129], v[218:219], off offset:1280 nt
	s_waitcnt lgkmcnt(0)
	s_barrier
	s_waitcnt vmcnt(40)
	v_cvt_pk_f16_f32 v140, v140, v141
	v_cvt_pk_f16_f32 v141, v142, v143
	v_cvt_pk_f16_f32 v144, v144, v145
	v_cvt_pk_f16_f32 v145, v146, v147
	v_cvt_pk_f16_f32 v148, v148, v149
	v_cvt_pk_f16_f32 v149, v150, v151
	v_cvt_pk_f16_f32 v152, v152, v153
	v_cvt_pk_f16_f32 v153, v154, v155
	v_cvt_pk_f16_f32 v156, v156, v157
	v_cvt_pk_f16_f32 v157, v158, v159
	v_cvt_pk_f16_f32 v160, v160, v161
	v_cvt_pk_f16_f32 v161, v162, v163
	v_cvt_pk_f16_f32 v164, v164, v165
	v_cvt_pk_f16_f32 v165, v166, v167
	v_cvt_pk_f16_f32 v168, v168, v169
	v_cvt_pk_f16_f32 v169, v170, v171
	ds_write_b64 v134, v[140:141] offset:8192
	ds_write_b64 v135, v[144:145] offset:8192
	ds_write_b64 v139, v[148:149] offset:8704
	ds_write_b64 v139, v[152:153] offset:8960
	ds_write_b64 v1, v[156:157] offset:8192
	ds_write_b64 v136, v[160:161] offset:8192
	ds_write_b64 v137, v[164:165] offset:8192
	ds_write_b64 v138, v[168:169] offset:8192
	global_load_dwordx4 v[140:143], v[204:205], off offset:1536 nt
	global_load_dwordx4 v[144:147], v[206:207], off offset:1536 nt
	global_load_dwordx4 v[148:151], v[208:209], off offset:1536 nt
	global_load_dwordx4 v[152:155], v[210:211], off offset:1536 nt
	global_load_dwordx4 v[156:159], v[212:213], off offset:1536 nt
	global_load_dwordx4 v[160:163], v[214:215], off offset:1536 nt
	global_load_dwordx4 v[164:167], v[216:217], off offset:1536 nt
	global_load_dwordx4 v[168:171], v[218:219], off offset:1536 nt
	s_waitcnt lgkmcnt(0)
	s_barrier
	s_waitcnt vmcnt(40)
	v_cvt_pk_f16_f32 v172, v172, v173
	v_cvt_pk_f16_f32 v173, v174, v175
	v_cvt_pk_f16_f32 v176, v176, v177
	v_cvt_pk_f16_f32 v177, v178, v179
	v_cvt_pk_f16_f32 v180, v180, v181
	v_cvt_pk_f16_f32 v181, v182, v183
	v_cvt_pk_f16_f32 v184, v184, v185
	v_cvt_pk_f16_f32 v185, v186, v187
	v_cvt_pk_f16_f32 v188, v188, v189
	v_cvt_pk_f16_f32 v189, v190, v191
	v_cvt_pk_f16_f32 v192, v192, v193
	v_cvt_pk_f16_f32 v193, v194, v195
	v_cvt_pk_f16_f32 v196, v196, v197
	v_cvt_pk_f16_f32 v197, v198, v199
	v_cvt_pk_f16_f32 v200, v200, v201
	v_cvt_pk_f16_f32 v201, v202, v203
	ds_write_b64 v134, v[172:173] offset:16384
	ds_write_b64 v135, v[176:177] offset:16384
	ds_write_b64 v139, v[180:181] offset:16896
	ds_write_b64 v139, v[184:185] offset:17152
	ds_write_b64 v1, v[188:189] offset:16384
	ds_write_b64 v136, v[192:193] offset:16384
	ds_write_b64 v137, v[196:197] offset:16384
	ds_write_b64 v138, v[200:201] offset:16384
	global_load_dwordx4 v[172:175], v[204:205], off offset:1792 nt
	global_load_dwordx4 v[176:179], v[206:207], off offset:1792 nt
	global_load_dwordx4 v[180:183], v[208:209], off offset:1792 nt
	global_load_dwordx4 v[184:187], v[210:211], off offset:1792 nt
	global_load_dwordx4 v[188:191], v[212:213], off offset:1792 nt
	global_load_dwordx4 v[192:195], v[214:215], off offset:1792 nt
	global_load_dwordx4 v[196:199], v[216:217], off offset:1792 nt
	global_load_dwordx4 v[200:203], v[218:219], off offset:1792 nt
	s_waitcnt lgkmcnt(0)
	s_barrier
	s_waitcnt vmcnt(40)
	v_cvt_pk_f16_f32 v2, v2, v3
	v_cvt_pk_f16_f32 v3, v4, v5
	v_cvt_pk_f16_f32 v6, v6, v7
	v_cvt_pk_f16_f32 v7, v8, v9
	v_cvt_pk_f16_f32 v10, v10, v11
	v_cvt_pk_f16_f32 v11, v12, v13
	v_cvt_pk_f16_f32 v14, v14, v15
	v_cvt_pk_f16_f32 v15, v16, v17
	v_cvt_pk_f16_f32 v18, v18, v19
	v_cvt_pk_f16_f32 v19, v20, v21
	v_cvt_pk_f16_f32 v22, v22, v23
	v_cvt_pk_f16_f32 v23, v24, v25
	v_cvt_pk_f16_f32 v26, v26, v27
	v_cvt_pk_f16_f32 v27, v28, v29
	v_cvt_pk_f16_f32 v30, v30, v31
	v_cvt_pk_f16_f32 v31, v32, v33
	ds_write_b64 v134, v[2:3]
	ds_write_b64 v135, v[6:7]
	ds_write_b64 v139, v[10:11] offset:512
	ds_write_b64 v139, v[14:15] offset:768
	ds_write_b64 v1, v[18:19]
	ds_write_b64 v136, v[22:23]
	ds_write_b64 v137, v[26:27]
	ds_write_b64 v138, v[30:31]
	global_load_dwordx4 v[2:5], v[204:205], off offset:2048 nt
	global_load_dwordx4 v[6:9], v[206:207], off offset:2048 nt
	global_load_dwordx4 v[10:13], v[208:209], off offset:2048 nt
	global_load_dwordx4 v[14:17], v[210:211], off offset:2048 nt
	global_load_dwordx4 v[18:21], v[212:213], off offset:2048 nt
	global_load_dwordx4 v[22:25], v[214:215], off offset:2048 nt
	global_load_dwordx4 v[26:29], v[216:217], off offset:2048 nt
	global_load_dwordx4 v[30:33], v[218:219], off offset:2048 nt
	s_waitcnt lgkmcnt(0)
	s_barrier
	s_waitcnt vmcnt(40)
	v_cvt_pk_f16_f32 v34, v34, v35
	v_cvt_pk_f16_f32 v35, v36, v37
	v_cvt_pk_f16_f32 v38, v38, v39
	v_cvt_pk_f16_f32 v39, v40, v41
	v_cvt_pk_f16_f32 v42, v42, v43
	v_cvt_pk_f16_f32 v43, v44, v45
	v_cvt_pk_f16_f32 v46, v46, v47
	v_cvt_pk_f16_f32 v47, v48, v49
	v_cvt_pk_f16_f32 v50, v50, v51
	v_cvt_pk_f16_f32 v51, v52, v53
	v_cvt_pk_f16_f32 v54, v54, v55
	v_cvt_pk_f16_f32 v55, v56, v57
	v_cvt_pk_f16_f32 v58, v58, v59
	v_cvt_pk_f16_f32 v59, v60, v61
	v_cvt_pk_f16_f32 v62, v62, v63
	v_cvt_pk_f16_f32 v63, v64, v65
	ds_write_b64 v134, v[34:35] offset:8192
	ds_write_b64 v135, v[38:39] offset:8192
	ds_write_b64 v139, v[42:43] offset:8704
	ds_write_b64 v139, v[46:47] offset:8960
	ds_write_b64 v1, v[50:51] offset:8192
	ds_write_b64 v136, v[54:55] offset:8192
	ds_write_b64 v137, v[58:59] offset:8192
	ds_write_b64 v138, v[62:63] offset:8192
	global_load_dwordx4 v[34:37], v[204:205], off offset:2304 nt
	global_load_dwordx4 v[38:41], v[206:207], off offset:2304 nt
	global_load_dwordx4 v[42:45], v[208:209], off offset:2304 nt
	global_load_dwordx4 v[46:49], v[210:211], off offset:2304 nt
	global_load_dwordx4 v[50:53], v[212:213], off offset:2304 nt
	global_load_dwordx4 v[54:57], v[214:215], off offset:2304 nt
	global_load_dwordx4 v[58:61], v[216:217], off offset:2304 nt
	global_load_dwordx4 v[62:65], v[218:219], off offset:2304 nt
	s_waitcnt lgkmcnt(0)
	s_barrier
	s_waitcnt vmcnt(40)
	v_cvt_pk_f16_f32 v66, v66, v67
	v_cvt_pk_f16_f32 v67, v68, v69
	v_cvt_pk_f16_f32 v70, v70, v71
	v_cvt_pk_f16_f32 v71, v72, v73
	v_cvt_pk_f16_f32 v74, v74, v75
	v_cvt_pk_f16_f32 v75, v76, v77
	v_cvt_pk_f16_f32 v78, v78, v79
	v_cvt_pk_f16_f32 v79, v80, v81
	v_cvt_pk_f16_f32 v82, v82, v83
	v_cvt_pk_f16_f32 v83, v84, v85
	v_cvt_pk_f16_f32 v86, v86, v87
	v_cvt_pk_f16_f32 v87, v88, v89
	v_cvt_pk_f16_f32 v90, v90, v91
	v_cvt_pk_f16_f32 v91, v92, v93
	v_cvt_pk_f16_f32 v94, v94, v95
	v_cvt_pk_f16_f32 v95, v96, v97
	ds_write_b64 v134, v[66:67] offset:16384
	ds_write_b64 v135, v[70:71] offset:16384
	ds_write_b64 v139, v[74:75] offset:16896
	ds_write_b64 v139, v[78:79] offset:17152
	ds_write_b64 v1, v[82:83] offset:16384
	ds_write_b64 v136, v[86:87] offset:16384
	ds_write_b64 v137, v[90:91] offset:16384
	ds_write_b64 v138, v[94:95] offset:16384
	global_load_dwordx4 v[66:69], v[204:205], off offset:2560 nt
	global_load_dwordx4 v[70:73], v[206:207], off offset:2560 nt
	global_load_dwordx4 v[74:77], v[208:209], off offset:2560 nt
	global_load_dwordx4 v[78:81], v[210:211], off offset:2560 nt
	global_load_dwordx4 v[82:85], v[212:213], off offset:2560 nt
	global_load_dwordx4 v[86:89], v[214:215], off offset:2560 nt
	global_load_dwordx4 v[90:93], v[216:217], off offset:2560 nt
	global_load_dwordx4 v[94:97], v[218:219], off offset:2560 nt
	s_waitcnt lgkmcnt(0)
	s_barrier
	s_waitcnt vmcnt(40)
	v_cvt_pk_f16_f32 v98, v98, v99
	v_cvt_pk_f16_f32 v99, v100, v101
	v_cvt_pk_f16_f32 v102, v102, v103
	v_cvt_pk_f16_f32 v103, v104, v105
	v_cvt_pk_f16_f32 v106, v106, v107
	v_cvt_pk_f16_f32 v107, v108, v109
	v_cvt_pk_f16_f32 v110, v110, v111
	v_cvt_pk_f16_f32 v111, v112, v113
	v_cvt_pk_f16_f32 v114, v114, v115
	v_cvt_pk_f16_f32 v115, v116, v117
	v_cvt_pk_f16_f32 v118, v118, v119
	v_cvt_pk_f16_f32 v119, v120, v121
	v_cvt_pk_f16_f32 v122, v122, v123
	v_cvt_pk_f16_f32 v123, v124, v125
	v_cvt_pk_f16_f32 v126, v126, v127
	v_cvt_pk_f16_f32 v127, v128, v129
	ds_write_b64 v134, v[98:99]
	ds_write_b64 v135, v[102:103]
	ds_write_b64 v139, v[106:107] offset:512
	ds_write_b64 v139, v[110:111] offset:768
	ds_write_b64 v1, v[114:115]
	ds_write_b64 v136, v[118:119]
	ds_write_b64 v137, v[122:123]
	ds_write_b64 v138, v[126:127]
	global_load_dwordx4 v[98:101], v[204:205], off offset:2816 nt
	global_load_dwordx4 v[102:105], v[206:207], off offset:2816 nt
	global_load_dwordx4 v[106:109], v[208:209], off offset:2816 nt
	global_load_dwordx4 v[110:113], v[210:211], off offset:2816 nt
	global_load_dwordx4 v[114:117], v[212:213], off offset:2816 nt
	global_load_dwordx4 v[118:121], v[214:215], off offset:2816 nt
	global_load_dwordx4 v[122:125], v[216:217], off offset:2816 nt
	global_load_dwordx4 v[126:129], v[218:219], off offset:2816 nt
	s_waitcnt lgkmcnt(0)
	s_barrier
	s_waitcnt vmcnt(40)
	v_cvt_pk_f16_f32 v140, v140, v141
	v_cvt_pk_f16_f32 v141, v142, v143
	v_cvt_pk_f16_f32 v144, v144, v145
	v_cvt_pk_f16_f32 v145, v146, v147
	v_cvt_pk_f16_f32 v148, v148, v149
	v_cvt_pk_f16_f32 v149, v150, v151
	v_cvt_pk_f16_f32 v152, v152, v153
	v_cvt_pk_f16_f32 v153, v154, v155
	v_cvt_pk_f16_f32 v156, v156, v157
	v_cvt_pk_f16_f32 v157, v158, v159
	v_cvt_pk_f16_f32 v160, v160, v161
	v_cvt_pk_f16_f32 v161, v162, v163
	v_cvt_pk_f16_f32 v164, v164, v165
	v_cvt_pk_f16_f32 v165, v166, v167
	v_cvt_pk_f16_f32 v168, v168, v169
	v_cvt_pk_f16_f32 v169, v170, v171
	ds_write_b64 v134, v[140:141] offset:8192
	ds_write_b64 v135, v[144:145] offset:8192
	ds_write_b64 v139, v[148:149] offset:8704
	ds_write_b64 v139, v[152:153] offset:8960
	ds_write_b64 v1, v[156:157] offset:8192
	ds_write_b64 v136, v[160:161] offset:8192
	ds_write_b64 v137, v[164:165] offset:8192
	ds_write_b64 v138, v[168:169] offset:8192
	global_load_dwordx4 v[140:143], v[204:205], off offset:3072 nt
	global_load_dwordx4 v[144:147], v[206:207], off offset:3072 nt
	global_load_dwordx4 v[148:151], v[208:209], off offset:3072 nt
	global_load_dwordx4 v[152:155], v[210:211], off offset:3072 nt
	global_load_dwordx4 v[156:159], v[212:213], off offset:3072 nt
	global_load_dwordx4 v[160:163], v[214:215], off offset:3072 nt
	global_load_dwordx4 v[164:167], v[216:217], off offset:3072 nt
	global_load_dwordx4 v[168:171], v[218:219], off offset:3072 nt
	s_waitcnt lgkmcnt(0)
	s_barrier
	s_waitcnt vmcnt(40)
	v_cvt_pk_f16_f32 v172, v172, v173
	v_cvt_pk_f16_f32 v173, v174, v175
	v_cvt_pk_f16_f32 v176, v176, v177
	v_cvt_pk_f16_f32 v177, v178, v179
	v_cvt_pk_f16_f32 v180, v180, v181
	v_cvt_pk_f16_f32 v181, v182, v183
	v_cvt_pk_f16_f32 v184, v184, v185
	v_cvt_pk_f16_f32 v185, v186, v187
	v_cvt_pk_f16_f32 v188, v188, v189
	v_cvt_pk_f16_f32 v189, v190, v191
	v_cvt_pk_f16_f32 v192, v192, v193
	v_cvt_pk_f16_f32 v193, v194, v195
	v_cvt_pk_f16_f32 v196, v196, v197
	v_cvt_pk_f16_f32 v197, v198, v199
	v_cvt_pk_f16_f32 v200, v200, v201
	v_cvt_pk_f16_f32 v201, v202, v203
	ds_write_b64 v134, v[172:173] offset:16384
	ds_write_b64 v135, v[176:177] offset:16384
	ds_write_b64 v139, v[180:181] offset:16896
	ds_write_b64 v139, v[184:185] offset:17152
	ds_write_b64 v1, v[188:189] offset:16384
	ds_write_b64 v136, v[192:193] offset:16384
	ds_write_b64 v137, v[196:197] offset:16384
	ds_write_b64 v138, v[200:201] offset:16384
	global_load_dwordx4 v[172:175], v[204:205], off offset:3328 nt
	global_load_dwordx4 v[176:179], v[206:207], off offset:3328 nt
	global_load_dwordx4 v[180:183], v[208:209], off offset:3328 nt
	global_load_dwordx4 v[184:187], v[210:211], off offset:3328 nt
	global_load_dwordx4 v[188:191], v[212:213], off offset:3328 nt
	global_load_dwordx4 v[192:195], v[214:215], off offset:3328 nt
	global_load_dwordx4 v[196:199], v[216:217], off offset:3328 nt
	global_load_dwordx4 v[200:203], v[218:219], off offset:3328 nt
	s_waitcnt lgkmcnt(0)
	s_barrier
	s_waitcnt vmcnt(40)
	v_cvt_pk_f16_f32 v2, v2, v3
	v_cvt_pk_f16_f32 v3, v4, v5
	v_cvt_pk_f16_f32 v6, v6, v7
	v_cvt_pk_f16_f32 v7, v8, v9
	v_cvt_pk_f16_f32 v10, v10, v11
	v_cvt_pk_f16_f32 v11, v12, v13
	v_cvt_pk_f16_f32 v14, v14, v15
	v_cvt_pk_f16_f32 v15, v16, v17
	v_cvt_pk_f16_f32 v18, v18, v19
	v_cvt_pk_f16_f32 v19, v20, v21
	v_cvt_pk_f16_f32 v22, v22, v23
	v_cvt_pk_f16_f32 v23, v24, v25
	v_cvt_pk_f16_f32 v26, v26, v27
	v_cvt_pk_f16_f32 v27, v28, v29
	v_cvt_pk_f16_f32 v30, v30, v31
	v_cvt_pk_f16_f32 v31, v32, v33
	ds_write_b64 v134, v[2:3]
	ds_write_b64 v135, v[6:7]
	ds_write_b64 v139, v[10:11] offset:512
	ds_write_b64 v139, v[14:15] offset:768
	ds_write_b64 v1, v[18:19]
	ds_write_b64 v136, v[22:23]
	ds_write_b64 v137, v[26:27]
	ds_write_b64 v138, v[30:31]
	global_load_dwordx4 v[2:5], v[204:205], off offset:3584 nt
	global_load_dwordx4 v[6:9], v[206:207], off offset:3584 nt
	global_load_dwordx4 v[10:13], v[208:209], off offset:3584 nt
	global_load_dwordx4 v[14:17], v[210:211], off offset:3584 nt
	global_load_dwordx4 v[18:21], v[212:213], off offset:3584 nt
	global_load_dwordx4 v[22:25], v[214:215], off offset:3584 nt
	global_load_dwordx4 v[26:29], v[216:217], off offset:3584 nt
	global_load_dwordx4 v[30:33], v[218:219], off offset:3584 nt
	s_waitcnt lgkmcnt(0)
	s_barrier
	s_waitcnt vmcnt(40)
	v_cvt_pk_f16_f32 v34, v34, v35
	v_cvt_pk_f16_f32 v35, v36, v37
	v_cvt_pk_f16_f32 v38, v38, v39
	v_cvt_pk_f16_f32 v39, v40, v41
	v_cvt_pk_f16_f32 v42, v42, v43
	v_cvt_pk_f16_f32 v43, v44, v45
	v_cvt_pk_f16_f32 v46, v46, v47
	v_cvt_pk_f16_f32 v47, v48, v49
	v_cvt_pk_f16_f32 v50, v50, v51
	v_cvt_pk_f16_f32 v51, v52, v53
	v_cvt_pk_f16_f32 v54, v54, v55
	v_cvt_pk_f16_f32 v55, v56, v57
	v_cvt_pk_f16_f32 v58, v58, v59
	v_cvt_pk_f16_f32 v59, v60, v61
	v_cvt_pk_f16_f32 v62, v62, v63
	v_cvt_pk_f16_f32 v63, v64, v65
	ds_write_b64 v134, v[34:35] offset:8192
	ds_write_b64 v135, v[38:39] offset:8192
	ds_write_b64 v139, v[42:43] offset:8704
	ds_write_b64 v139, v[46:47] offset:8960
	ds_write_b64 v1, v[50:51] offset:8192
	ds_write_b64 v136, v[54:55] offset:8192
	ds_write_b64 v137, v[58:59] offset:8192
	ds_write_b64 v138, v[62:63] offset:8192
	global_load_dwordx4 v[34:37], v[204:205], off offset:3840 nt
	global_load_dwordx4 v[38:41], v[206:207], off offset:3840 nt
	global_load_dwordx4 v[42:45], v[208:209], off offset:3840 nt
	global_load_dwordx4 v[46:49], v[210:211], off offset:3840 nt
	global_load_dwordx4 v[50:53], v[212:213], off offset:3840 nt
	global_load_dwordx4 v[54:57], v[214:215], off offset:3840 nt
	global_load_dwordx4 v[58:61], v[216:217], off offset:3840 nt
	global_load_dwordx4 v[62:65], v[218:219], off offset:3840 nt
	s_waitcnt lgkmcnt(0)
	s_barrier
	s_waitcnt vmcnt(40)
	v_cvt_pk_f16_f32 v66, v66, v67
	v_cvt_pk_f16_f32 v67, v68, v69
	v_cvt_pk_f16_f32 v70, v70, v71
	v_cvt_pk_f16_f32 v71, v72, v73
	v_cvt_pk_f16_f32 v74, v74, v75
	v_cvt_pk_f16_f32 v75, v76, v77
	v_cvt_pk_f16_f32 v78, v78, v79
	v_cvt_pk_f16_f32 v79, v80, v81
	v_cvt_pk_f16_f32 v82, v82, v83
	v_cvt_pk_f16_f32 v83, v84, v85
	v_cvt_pk_f16_f32 v86, v86, v87
	v_cvt_pk_f16_f32 v87, v88, v89
	v_cvt_pk_f16_f32 v90, v90, v91
	v_cvt_pk_f16_f32 v91, v92, v93
	v_cvt_pk_f16_f32 v94, v94, v95
	v_cvt_pk_f16_f32 v95, v96, v97
	ds_write_b64 v134, v[66:67] offset:16384
	ds_write_b64 v135, v[70:71] offset:16384
	ds_write_b64 v139, v[74:75] offset:16896
	ds_write_b64 v139, v[78:79] offset:17152
	ds_write_b64 v1, v[82:83] offset:16384
	ds_write_b64 v136, v[86:87] offset:16384
	ds_write_b64 v137, v[90:91] offset:16384
	ds_write_b64 v138, v[94:95] offset:16384
	s_waitcnt lgkmcnt(0)
	s_barrier
	s_waitcnt vmcnt(32)
	v_cvt_pk_f16_f32 v98, v98, v99
	v_cvt_pk_f16_f32 v99, v100, v101
	v_cvt_pk_f16_f32 v102, v102, v103
	v_cvt_pk_f16_f32 v103, v104, v105
	v_cvt_pk_f16_f32 v106, v106, v107
	v_cvt_pk_f16_f32 v107, v108, v109
	v_cvt_pk_f16_f32 v110, v110, v111
	v_cvt_pk_f16_f32 v111, v112, v113
	v_cvt_pk_f16_f32 v114, v114, v115
	v_cvt_pk_f16_f32 v115, v116, v117
	v_cvt_pk_f16_f32 v118, v118, v119
	v_cvt_pk_f16_f32 v119, v120, v121
	v_cvt_pk_f16_f32 v122, v122, v123
	v_cvt_pk_f16_f32 v123, v124, v125
	v_cvt_pk_f16_f32 v126, v126, v127
	v_cvt_pk_f16_f32 v127, v128, v129
	ds_write_b64 v134, v[98:99]
	ds_write_b64 v135, v[102:103]
	ds_write_b64 v139, v[106:107] offset:512
	ds_write_b64 v139, v[110:111] offset:768
	ds_write_b64 v1, v[114:115]
	ds_write_b64 v136, v[118:119]
	ds_write_b64 v137, v[122:123]
	ds_write_b64 v138, v[126:127]
	s_waitcnt lgkmcnt(0)
	s_barrier
	s_waitcnt vmcnt(24)
	v_cvt_pk_f16_f32 v140, v140, v141
	v_cvt_pk_f16_f32 v141, v142, v143
	v_cvt_pk_f16_f32 v144, v144, v145
	v_cvt_pk_f16_f32 v145, v146, v147
	v_cvt_pk_f16_f32 v148, v148, v149
	v_cvt_pk_f16_f32 v149, v150, v151
	v_cvt_pk_f16_f32 v152, v152, v153
	v_cvt_pk_f16_f32 v153, v154, v155
	v_cvt_pk_f16_f32 v156, v156, v157
	v_cvt_pk_f16_f32 v157, v158, v159
	v_cvt_pk_f16_f32 v160, v160, v161
	v_cvt_pk_f16_f32 v161, v162, v163
	v_cvt_pk_f16_f32 v164, v164, v165
	v_cvt_pk_f16_f32 v165, v166, v167
	v_cvt_pk_f16_f32 v168, v168, v169
	v_cvt_pk_f16_f32 v169, v170, v171
	ds_write_b64 v134, v[140:141] offset:8192
	ds_write_b64 v135, v[144:145] offset:8192
	ds_write_b64 v139, v[148:149] offset:8704
	ds_write_b64 v139, v[152:153] offset:8960
	ds_write_b64 v1, v[156:157] offset:8192
	ds_write_b64 v136, v[160:161] offset:8192
	ds_write_b64 v137, v[164:165] offset:8192
	ds_write_b64 v138, v[168:169] offset:8192
	s_waitcnt lgkmcnt(0)
	s_barrier
	s_waitcnt vmcnt(16)
	v_cvt_pk_f16_f32 v172, v172, v173
	v_cvt_pk_f16_f32 v173, v174, v175
	v_cvt_pk_f16_f32 v176, v176, v177
	v_cvt_pk_f16_f32 v177, v178, v179
	v_cvt_pk_f16_f32 v180, v180, v181
	v_cvt_pk_f16_f32 v181, v182, v183
	v_cvt_pk_f16_f32 v184, v184, v185
	v_cvt_pk_f16_f32 v185, v186, v187
	v_cvt_pk_f16_f32 v188, v188, v189
	v_cvt_pk_f16_f32 v189, v190, v191
	v_cvt_pk_f16_f32 v192, v192, v193
	v_cvt_pk_f16_f32 v193, v194, v195
	v_cvt_pk_f16_f32 v196, v196, v197
	v_cvt_pk_f16_f32 v197, v198, v199
	v_cvt_pk_f16_f32 v200, v200, v201
	v_cvt_pk_f16_f32 v201, v202, v203
	ds_write_b64 v134, v[172:173] offset:16384
	ds_write_b64 v135, v[176:177] offset:16384
	ds_write_b64 v139, v[180:181] offset:16896
	ds_write_b64 v139, v[184:185] offset:17152
	ds_write_b64 v1, v[188:189] offset:16384
	ds_write_b64 v136, v[192:193] offset:16384
	ds_write_b64 v137, v[196:197] offset:16384
	ds_write_b64 v138, v[200:201] offset:16384
	s_waitcnt lgkmcnt(0)
	s_barrier
	s_waitcnt vmcnt(8)
	v_cvt_pk_f16_f32 v2, v2, v3
	v_cvt_pk_f16_f32 v3, v4, v5
	v_cvt_pk_f16_f32 v6, v6, v7
	v_cvt_pk_f16_f32 v7, v8, v9
	v_cvt_pk_f16_f32 v10, v10, v11
	v_cvt_pk_f16_f32 v11, v12, v13
	v_cvt_pk_f16_f32 v14, v14, v15
	v_cvt_pk_f16_f32 v15, v16, v17
	v_cvt_pk_f16_f32 v18, v18, v19
	v_cvt_pk_f16_f32 v19, v20, v21
	v_cvt_pk_f16_f32 v22, v22, v23
	v_cvt_pk_f16_f32 v23, v24, v25
	v_cvt_pk_f16_f32 v26, v26, v27
	v_cvt_pk_f16_f32 v27, v28, v29
	v_cvt_pk_f16_f32 v30, v30, v31
	v_cvt_pk_f16_f32 v31, v32, v33
	ds_write_b64 v134, v[2:3]
	ds_write_b64 v135, v[6:7]
	ds_write_b64 v139, v[10:11] offset:512
	ds_write_b64 v139, v[14:15] offset:768
	ds_write_b64 v1, v[18:19]
	ds_write_b64 v136, v[22:23]
	ds_write_b64 v137, v[26:27]
	ds_write_b64 v138, v[30:31]
	s_waitcnt lgkmcnt(0)
	s_barrier
	s_waitcnt vmcnt(0)
	v_cvt_pk_f16_f32 v34, v34, v35
	v_cvt_pk_f16_f32 v35, v36, v37
	v_cvt_pk_f16_f32 v38, v38, v39
	v_cvt_pk_f16_f32 v39, v40, v41
	v_cvt_pk_f16_f32 v42, v42, v43
	v_cvt_pk_f16_f32 v43, v44, v45
	v_cvt_pk_f16_f32 v46, v46, v47
	v_cvt_pk_f16_f32 v47, v48, v49
	v_cvt_pk_f16_f32 v50, v50, v51
	v_cvt_pk_f16_f32 v51, v52, v53
	v_cvt_pk_f16_f32 v54, v54, v55
	v_cvt_pk_f16_f32 v55, v56, v57
	v_cvt_pk_f16_f32 v58, v58, v59
	v_cvt_pk_f16_f32 v59, v60, v61
	v_cvt_pk_f16_f32 v62, v62, v63
	v_cvt_pk_f16_f32 v63, v64, v65
	ds_write_b64 v134, v[34:35] offset:8192
	ds_write_b64 v135, v[38:39] offset:8192
	ds_write_b64 v139, v[42:43] offset:8704
	ds_write_b64 v139, v[46:47] offset:8960
	ds_write_b64 v1, v[50:51] offset:8192
	ds_write_b64 v136, v[54:55] offset:8192
	ds_write_b64 v137, v[58:59] offset:8192
	ds_write_b64 v138, v[62:63] offset:8192
	s_waitcnt lgkmcnt(0)
	s_barrier

.LBB2_11:
	s_load_dwordx2 s[0:1], s[0:1], 0x0
	s_ashr_i32 s4, s2, 7
	s_ashr_i32 s5, s4, 31
	s_lshl_b64 s[4:5], s[4:5], 21
	v_lshlrev_b32_e32 v1, 4, v0
	s_waitcnt lgkmcnt(0)
	s_add_u32 s0, s0, s4
	s_addc_u32 s2, s1, s5
	s_lshl_b32 s4, s14, 1
	s_waitcnt vmcnt(6)
	v_and_b32_e32 v2, 32, v0
	s_add_u32 s4, s0, s4
	v_bitop3_b32 v1, v1, v2, 48 bitop3:0x6c
	v_lshlrev_b32_e32 v0, 11, v0
	s_mov_b32 s0, 0x1e000
	s_mov_b32 s1, 0
	s_addc_u32 s5, s2, 0
	v_and_or_b32 v0, v0, s0, v1
	s_add_i32 s0, s3, -6
	s_lshl_b64 s[2:3], s[0:1], 20
	s_add_u32 s2, s4, s2
	s_addc_u32 s3, s5, s3
	s_lshl_b32 s0, s0, 14
	v_mov_b32_e32 v1, 0
	v_lshl_add_u64 v[16:17], s[2:3], 0, v[0:1]
	s_mov_b32 m0, s0
	v_or_b32_e32 v2, 0x20000, v0
	global_load_lds_dwordx4 v0, s[2:3]
	v_lshl_add_u64 v[18:19], v[16:17], 0, 64
	s_or_b32 m0, s0, 0x400
	v_mov_b32_e32 v3, v1
	global_load_lds_dwordx4 v[18:19], off
	v_lshl_add_u64 v[18:19], s[2:3], 0, v[2:3]
	s_or_b32 m0, s0, 0x800
	v_or_b32_e32 v4, 0x40000, v0
	global_load_lds_dwordx4 v2, s[2:3]
	v_lshl_add_u64 v[20:21], v[18:19], 0, 64
	s_or_b32 m0, s0, 0xc00
	v_mov_b32_e32 v5, v1
	global_load_lds_dwordx4 v[20:21], off
	v_lshl_add_u64 v[20:21], s[2:3], 0, v[4:5]
	s_or_b32 m0, s0, 0x1000
	v_or_b32_e32 v6, 0x60000, v0
	global_load_lds_dwordx4 v4, s[2:3]
	v_lshl_add_u64 v[22:23], v[20:21], 0, 64
	s_or_b32 m0, s0, 0x1400
	v_mov_b32_e32 v7, v1
	global_load_lds_dwordx4 v[22:23], off
	v_lshl_add_u64 v[22:23], s[2:3], 0, v[6:7]
	s_or_b32 m0, s0, 0x1800
	v_or_b32_e32 v8, 0x80000, v0
	global_load_lds_dwordx4 v6, s[2:3]
	v_lshl_add_u64 v[24:25], v[22:23], 0, 64
	s_or_b32 m0, s0, 0x1c00
	v_mov_b32_e32 v9, v1
	global_load_lds_dwordx4 v[24:25], off
	v_lshl_add_u64 v[24:25], s[2:3], 0, v[8:9]
	s_or_b32 m0, s0, 0x2000
	v_or_b32_e32 v10, 0xa0000, v0
	global_load_lds_dwordx4 v8, s[2:3]
	v_lshl_add_u64 v[26:27], v[24:25], 0, 64
	s_or_b32 m0, s0, 0x2400
	v_mov_b32_e32 v11, v1
	global_load_lds_dwordx4 v[26:27], off
	v_lshl_add_u64 v[26:27], s[2:3], 0, v[10:11]
	s_or_b32 m0, s0, 0x2800
	v_or_b32_e32 v12, 0xc0000, v0
	global_load_lds_dwordx4 v10, s[2:3]
	v_lshl_add_u64 v[28:29], v[26:27], 0, 64
	s_or_b32 m0, s0, 0x2c00
	v_mov_b32_e32 v13, v1
	global_load_lds_dwordx4 v[28:29], off
	v_lshl_add_u64 v[28:29], s[2:3], 0, v[12:13]
	s_or_b32 m0, s0, 0x3000
	v_lshl_add_u64 v[30:31], v[28:29], 0, 64
	global_load_lds_dwordx4 v12, s[2:3]
	s_or_b32 m0, s0, 0x3400
	v_or_b32_e32 v14, 0xe0000, v0
	global_load_lds_dwordx4 v[30:31], off
	v_mov_b32_e32 v15, v1
	s_or_b32 m0, s0, 0x3800
	v_lshl_add_u64 v[30:31], s[2:3], 0, v[14:15]
	global_load_lds_dwordx4 v14, s[2:3]
	s_or_b32 m0, s0, 0x3c00
	v_lshl_add_u64 v[32:33], v[30:31], 0, 64
	s_mov_b64 s[4:5], 0x80
	s_add_u32 s6, s2, 0x80
	global_load_lds_dwordx4 v[32:33], off
	s_addc_u32 s7, s3, 0
	s_add_i32 m0, s0, 0x8000
	v_lshl_add_u64 v[32:33], v[16:17], 0, s[4:5]
	s_mov_b64 s[4:5], 0xc0
	global_load_lds_dwordx4 v[32:33], off
	v_lshl_add_u64 v[16:17], v[16:17], 0, s[4:5]
	s_add_i32 m0, s0, 0x8400
	s_mov_b32 s8, 0x10000
	global_load_lds_dwordx4 v[16:17], off
	s_add_i32 m0, s0, 0x8800
	v_lshl_add_u64 v[16:17], v[18:19], 0, s[4:5]
	global_load_lds_dwordx4 v2, s[6:7]
	s_add_i32 m0, s0, 0x8c00
	s_nop 0
	global_load_lds_dwordx4 v[16:17], off
	s_add_i32 m0, s0, 0x9000
	v_lshl_add_u64 v[16:17], v[20:21], 0, s[4:5]
	global_load_lds_dwordx4 v4, s[6:7]
	s_add_i32 m0, s0, 0x9400
	s_nop 0
	global_load_lds_dwordx4 v[16:17], off
	s_add_i32 m0, s0, 0x9800
	v_lshl_add_u64 v[16:17], v[22:23], 0, s[4:5]
	global_load_lds_dwordx4 v6, s[6:7]
	s_add_i32 m0, s0, 0x9c00
	s_nop 0
	global_load_lds_dwordx4 v[16:17], off
	s_add_i32 m0, s0, 0xa000
	v_lshl_add_u64 v[16:17], v[24:25], 0, s[4:5]
	global_load_lds_dwordx4 v8, s[6:7]
	s_add_i32 m0, s0, 0xa400
	s_nop 0
	global_load_lds_dwordx4 v[16:17], off
	s_add_i32 m0, s0, 0xa800
	v_lshl_add_u64 v[16:17], v[26:27], 0, s[4:5]
	global_load_lds_dwordx4 v10, s[6:7]
	s_add_i32 m0, s0, 0xac00
	s_nop 0
	global_load_lds_dwordx4 v[16:17], off
	s_add_i32 m0, s0, 0xb000
	v_lshl_add_u64 v[16:17], v[28:29], 0, s[4:5]
	global_load_lds_dwordx4 v12, s[6:7]
	s_add_i32 m0, s0, 0xb400
	s_nop 0
	global_load_lds_dwordx4 v[16:17], off
	s_add_i32 m0, s0, 0xb800
	v_lshl_add_u64 v[16:17], v[30:31], 0, s[4:5]
	global_load_lds_dwordx4 v14, s[6:7]
	s_add_i32 m0, s0, 0xbc00
	s_mov_b64 s[4:5], 0x100
	global_load_lds_dwordx4 v[16:17], off
	s_mov_b64 s[6:7], 0x140

	.amdhsa_kernel _Z6kv1s_k5RArgs
		.amdhsa_group_segment_fixed_size 122880
		.amdhsa_private_segment_fixed_size 0
		.amdhsa_kernarg_size 88
		.amdhsa_user_sgpr_count 2
		.amdhsa_user_sgpr_dispatch_ptr 0
		.amdhsa_user_sgpr_queue_ptr 0
		.amdhsa_user_sgpr_kernarg_segment_ptr 1
		.amdhsa_user_sgpr_dispatch_id 0
		.amdhsa_user_sgpr_kernarg_preload_length 0
		.amdhsa_user_sgpr_kernarg_preload_offset 0
		.amdhsa_user_sgpr_private_segment_size 0
		.amdhsa_uses_dynamic_stack 0
		.amdhsa_enable_private_segment 0
		.amdhsa_system_sgpr_workgroup_id_x 1
		.amdhsa_system_sgpr_workgroup_id_y 0
		.amdhsa_system_sgpr_workgroup_id_z 0
		.amdhsa_system_sgpr_workgroup_info 0
		.amdhsa_system_vgpr_workitem_id 0
		.amdhsa_next_free_vgpr 220
		.amdhsa_next_free_sgpr 96
		.amdhsa_accum_offset 220
		.amdhsa_reserve_vcc 1
		.amdhsa_float_round_mode_32 0
		.amdhsa_float_round_mode_16_64 0
		.amdhsa_float_denorm_mode_32 3
		.amdhsa_float_denorm_mode_16_64 3
		.amdhsa_dx10_clamp 1
		.amdhsa_ieee_mode 1
		.amdhsa_fp16_overflow 0
		.amdhsa_tg_split 0
		.amdhsa_exception_fp_ieee_invalid_op 0
		.amdhsa_exception_fp_denorm_src 0
		.amdhsa_exception_fp_ieee_div_zero 0
		.amdhsa_exception_fp_ieee_overflow 0
		.amdhsa_exception_fp_ieee_underflow 0
		.amdhsa_exception_fp_ieee_inexact 0
		.amdhsa_exception_int_div_zero 0
	.end_amdhsa_kernel

	.text
	.protected	_Z7k_phaseIN3pg86EpiOutEEvNS0_4GemmET_
	.globl	_Z7k_phaseIN3pg86EpiOutEEvNS0_4GemmET_
	.p2align	8
	.type	_Z7k_phaseIN3pg86EpiOutEEvNS0_4GemmET_,@function

	.amdhsa_kernel _Z7k_phaseIN3pg86EpiOutEEvNS0_4GemmET_
		.amdhsa_group_segment_fixed_size 131072
		.amdhsa_private_segment_fixed_size 0
		.amdhsa_kernarg_size 304
		.amdhsa_user_sgpr_count 2
		.amdhsa_user_sgpr_dispatch_ptr 0
		.amdhsa_user_sgpr_queue_ptr 0
		.amdhsa_user_sgpr_kernarg_segment_ptr 1
		.amdhsa_user_sgpr_dispatch_id 0
		.amdhsa_user_sgpr_kernarg_preload_length 0
		.amdhsa_user_sgpr_kernarg_preload_offset 0
		.amdhsa_user_sgpr_private_segment_size 0
		.amdhsa_uses_dynamic_stack 0
		.amdhsa_enable_private_segment 0
		.amdhsa_system_sgpr_workgroup_id_x 1
		.amdhsa_system_sgpr_workgroup_id_y 0
		.amdhsa_system_sgpr_workgroup_id_z 0
		.amdhsa_system_sgpr_workgroup_info 0
		.amdhsa_system_vgpr_workitem_id 0
		.amdhsa_next_free_vgpr 238
		.amdhsa_next_free_sgpr 96
		.amdhsa_accum_offset 240
		.amdhsa_reserve_vcc 1
		.amdhsa_float_round_mode_32 0
		.amdhsa_float_round_mode_16_64 0
		.amdhsa_float_denorm_mode_32 3
		.amdhsa_float_denorm_mode_16_64 3
		.amdhsa_dx10_clamp 1
		.amdhsa_ieee_mode 1
		.amdhsa_fp16_overflow 0
		.amdhsa_tg_split 0
		.amdhsa_exception_fp_ieee_invalid_op 0
		.amdhsa_exception_fp_denorm_src 0
		.amdhsa_exception_fp_ieee_div_zero 0
		.amdhsa_exception_fp_ieee_overflow 0
		.amdhsa_exception_fp_ieee_underflow 0
		.amdhsa_exception_fp_ieee_inexact 0
		.amdhsa_exception_int_div_zero 0
	.end_amdhsa_kernel
	.text
.Lfunc_end6:
	.size	_Z7k_phaseIN3pg86EpiOutEEvNS0_4GemmET_, .Lfunc_end6-_Z7k_phaseIN3pg86EpiOutEEvNS0_4GemmET_
	.set _Z7k_phaseIN3pg86EpiOutEEvNS0_4GemmET_.num_vgpr, 238
	.set _Z7k_phaseIN3pg86EpiOutEEvNS0_4GemmET_.num_agpr, 0
	.set _Z7k_phaseIN3pg86EpiOutEEvNS0_4GemmET_.numbered_sgpr, 78
	.set _Z7k_phaseIN3pg86EpiOutEEvNS0_4GemmET_.num_named_barrier, 0
	.set _Z7k_phaseIN3pg86EpiOutEEvNS0_4GemmET_.private_seg_size, 0
	.set _Z7k_phaseIN3pg86EpiOutEEvNS0_4GemmET_.uses_vcc, 1
	.set _Z7k_phaseIN3pg86EpiOutEEvNS0_4GemmET_.uses_flat_scratch, 0
	.set _Z7k_phaseIN3pg86EpiOutEEvNS0_4GemmET_.has_dyn_sized_stack, 0
	.set _Z7k_phaseIN3pg86EpiOutEEvNS0_4GemmET_.has_recursion, 0
	.set _Z7k_phaseIN3pg86EpiOutEEvNS0_4GemmET_.has_indirect_call, 0

amdhsa.kernels:
  - .agpr_count:     0
    .args:
      - .offset:         0
        .size:           120
        .value_kind:     by_value
    .group_segment_fixed_size: 16640
    .kernarg_segment_align: 8
    .kernarg_segment_size: 120
    .language:       OpenCL C
    .language_version:
      - 2
      - 0
    .max_flat_workgroup_size: 256
    .name:           _Z8prep_all5PArgs
    .private_segment_fixed_size: 0
    .sgpr_count:     45
    .sgpr_spill_count: 0
    .symbol:         _Z8prep_all5PArgs.kd
    .uniform_work_group_size: 1
    .uses_dynamic_stack: false
    .vgpr_count:     42
    .vgpr_spill_count: 0
    .wavefront_size: 64
  - .agpr_count:     0
    .args:
      - .actual_access:  read_only
        .address_space:  global
        .offset:         0
        .size:           8
        .value_kind:     global_buffer
      - .actual_access:  write_only
        .address_space:  global
        .offset:         8
        .size:           8
        .value_kind:     global_buffer
      - .actual_access:  read_only
        .address_space:  global
        .offset:         16
        .size:           8
        .value_kind:     global_buffer
      - .actual_access:  write_only
        .address_space:  global
        .offset:         24
        .size:           8
        .value_kind:     global_buffer
    .group_segment_fixed_size: 0
    .kernarg_segment_align: 8
    .kernarg_segment_size: 32
    .language:       OpenCL C
    .language_version:
      - 2
      - 0
    .max_flat_workgroup_size: 256
    .name:           _Z12reduce_slabsPKfPDF16_S0_Pf
    .private_segment_fixed_size: 0
    .sgpr_count:     17
    .sgpr_spill_count: 0
    .symbol:         _Z12reduce_slabsPKfPDF16_S0_Pf.kd
    .uniform_work_group_size: 1
    .uses_dynamic_stack: false
    .vgpr_count:     26
    .vgpr_spill_count: 0
    .wavefront_size: 64
  - .agpr_count:     0
    .args:
      - .offset:         0
        .size:           88
        .value_kind:     by_value
    .group_segment_fixed_size: 122880
    .kernarg_segment_align: 8
    .kernarg_segment_size: 88
    .language:       OpenCL C
    .language_version:
      - 2
      - 0
    .max_flat_workgroup_size: 512
    .name:           _Z6kv1s_k5RArgs
    .private_segment_fixed_size: 0
    .sgpr_count:     29
    .sgpr_spill_count: 0
    .symbol:         _Z6kv1s_k5RArgs.kd
    .uniform_work_group_size: 1
    .uses_dynamic_stack: false
    .vgpr_count:     220
    .vgpr_spill_count: 0
    .wavefront_size: 64
  - .agpr_count:     0
    .args:
      - .offset:         0
        .size:           88
        .value_kind:     by_value
      - .offset:         88
        .size:           32
        .value_kind:     by_value
      - .offset:         120
        .size:           16
        .value_kind:     by_value
    .group_segment_fixed_size: 131072
    .kernarg_segment_align: 8
    .kernarg_segment_size: 136
    .language:       OpenCL C
    .language_version:
      - 2
      - 0
    .max_flat_workgroup_size: 512
    .name:           _Z8k_kv2_qg5RArgsN3pg84GemmENS0_5EpiQTE
    .private_segment_fixed_size: 0
    .sgpr_count:     96
    .sgpr_spill_count: 0
    .symbol:         _Z8k_kv2_qg5RArgsN3pg84GemmENS0_5EpiQTE.kd
    .uniform_work_group_size: 1
    .uses_dynamic_stack: false
    .vgpr_count:     242
    .vgpr_spill_count: 0
    .wavefront_size: 64
  - .agpr_count:     0
    .args:
      - .offset:         0
        .size:           88
        .value_kind:     by_value
      - .offset:         88
        .size:           32
        .value_kind:     by_value
      - .offset:         120
        .size:           16
        .value_kind:     by_value
    .group_segment_fixed_size: 147456
    .kernarg_segment_align: 8
    .kernarg_segment_size: 136
    .language:       OpenCL C
    .language_version:
      - 2
      - 0
    .max_flat_workgroup_size: 512
    .name:           _Z8k_kv1_qg5RArgsN3pg84GemmENS0_5EpiQTE
    .private_segment_fixed_size: 0
    .sgpr_count:     82
    .sgpr_spill_count: 0
    .symbol:         _Z8k_kv1_qg5RArgsN3pg84GemmENS0_5EpiQTE.kd
    .uniform_work_group_size: 1
    .uses_dynamic_stack: false
    .vgpr_count:     242
    .vgpr_spill_count: 0
    .wavefront_size: 64
  - .agpr_count:     0
    .args:
      - .actual_access:  read_only
        .address_space:  global
        .offset:         0
        .size:           8
        .value_kind:     global_buffer
      - .actual_access:  read_only
        .address_space:  global
        .offset:         8
        .size:           8
        .value_kind:     global_buffer
      - .actual_access:  read_only
        .address_space:  global
        .offset:         16
        .size:           8
        .value_kind:     global_buffer
      - .actual_access:  write_only
        .address_space:  global
        .offset:         24
        .size:           8
        .value_kind:     global_buffer
    .group_segment_fixed_size: 102400
    .kernarg_segment_align: 8
    .kernarg_segment_size: 32
    .language:       OpenCL C
    .language_version:
      - 2
      - 0
    .max_flat_workgroup_size: 512
    .name:           _Z6attn_kPKDF16_S0_S0_PDF16_
    .private_segment_fixed_size: 0
    .sgpr_count:     19
    .sgpr_spill_count: 0
    .symbol:         _Z6attn_kPKDF16_S0_S0_PDF16_.kd
    .uniform_work_group_size: 1
    .uses_dynamic_stack: false
    .vgpr_count:     222
    .vgpr_spill_count: 0
    .wavefront_size: 64
  - .agpr_count:     0
    .args:
      - .offset:         0
        .size:           32
        .value_kind:     by_value
      - .offset:         32
        .size:           16
        .value_kind:     by_value
      - .offset:         48
        .size:           4
        .value_kind:     hidden_block_count_x
      - .offset:         52
        .size:           4
        .value_kind:     hidden_block_count_y
      - .offset:         56
        .size:           4
        .value_kind:     hidden_block_count_z
      - .offset:         60
        .size:           2
        .value_kind:     hidden_group_size_x
      - .offset:         62
        .size:           2
        .value_kind:     hidden_group_size_y
      - .offset:         64
        .size:           2
        .value_kind:     hidden_group_size_z
      - .offset:         66
        .size:           2
        .value_kind:     hidden_remainder_x
      - .offset:         68
        .size:           2
        .value_kind:     hidden_remainder_y
      - .offset:         70
        .size:           2
        .value_kind:     hidden_remainder_z
      - .offset:         88
        .size:           8
        .value_kind:     hidden_global_offset_x
      - .offset:         96
        .size:           8
        .value_kind:     hidden_global_offset_y
      - .offset:         104
        .size:           8
        .value_kind:     hidden_global_offset_z
      - .offset:         112
        .size:           2
        .value_kind:     hidden_grid_dims
    .group_segment_fixed_size: 131072
    .kernarg_segment_align: 8
    .kernarg_segment_size: 304
    .language:       OpenCL C
    .language_version:
      - 2
      - 0
    .max_flat_workgroup_size: 512
    .name:           _Z7k_phaseIN3pg86EpiOutEEvNS0_4GemmET_
    .private_segment_fixed_size: 0
    .sgpr_count:     84
    .sgpr_spill_count: 0
    .symbol:         _Z7k_phaseIN3pg86EpiOutEEvNS0_4GemmET_.kd
    .uniform_work_group_size: 1
    .uses_dynamic_stack: false
    .vgpr_count:     238
    .vgpr_spill_count: 0
    .wavefront_size: 64
